# w_in GEMM epilogue: the seven per-row scale loads are issued with the first loads at epilogue entry (before the int-to-float conversions) instead of immediately before the wait
# speedup vs baseline: 1.0108x; 1.0064x over previous
;     __device__ __forceinline__ void operator()(const f32x4 (&acc)[2][2][4][2], const Unit& u, int wr, int wc, int fr, int fq) const {
;         const bool swapped = (u.a1 >= 4 && u.a1 < 8);
;         const float* sA = swapped ? wsc + u.a1 * BM : xsc + u.a0 * BM; const float* sB = swapped ? xsc + u.a0 * BM : wsc + u.a1 * BM;
;         const int row0 = wr * 64 + fr, col0 = wc * 32 + 8 * fq;
;         if (u.ldc == 0) {
;             if (wc == 0 && fq < 2) { float* g = (float*)u.O; const f32x4 b0 = *(const f32x4*)(bif + 8 * fq), b1 = *(const f32x4*)(bif + 8 * fq + 4); const f32x4 s0 = *(const f32x4*)(sB + 8 * fq), s1 = *(const f32x4*)(sB + 8 * fq + 4);
; #pragma unroll
;                 for (int ai = 0; ai < 2; ++ai)
; #pragma unroll
;                     for (int m = 0; m < 4; ++m) { const int r = row0 + ai * HALF + m * 16; const float sr = sA[r]; float* rp = g + (size_t)r * 16 + 8 * fq;
;                         const i32x4_t a0 = __builtin_bit_cast(i32x4_t, acc[ai][0][m][0]), a1 = __builtin_bit_cast(i32x4_t, acc[ai][0][m][1]);
;                         *(f32x4*)rp = __builtin_convertvector(a0, f32x4) * sr * s0 + b0; *(f32x4*)(rp + 4) = __builtin_convertvector(a1, f32x4) * sr * s1 + b1; } }
;             return; }
;         bf16_t* base = (bf16_t*)u.O; const int ldc = u.ldc;
;         f32x4 sb[2][2];
; #pragma unroll
;         for (int bj = 0; bj < 2; ++bj)
; #pragma unroll
;             for (int n = 0; n < 2; ++n) sb[bj][n] = *(const f32x4*)(sB + col0 + bj * HALF + 4 * n);
;         if (u.a1 >= 16) {
; #pragma unroll
;             for (int ai = 0; ai < 2; ++ai)
; #pragma unroll
;                 for (int m = 0; m < 4; ++m) { const int r = row0 + ai * HALF + m * 16; const float sr = sA[r];
;                     const f32x4 p0 = (__builtin_convertvector(__builtin_bit_cast(i32x4_t, acc[ai][0][m][0]), f32x4) * sr * sb[0][0]) * (__builtin_convertvector(__builtin_bit_cast(i32x4_t, acc[ai][1][m][0]), f32x4) * sr * sb[1][0]);
;                     const f32x4 p1 = (__builtin_convertvector(__builtin_bit_cast(i32x4_t, acc[ai][0][m][1]), f32x4) * sr * sb[0][1]) * (__builtin_convertvector(__builtin_bit_cast(i32x4_t, acc[ai][1][m][1]), f32x4) * sr * sb[1][1]);
;                     u32x4 w; w.x = pk2(p0[0], p0[1]); w.y = pk2(p0[2], p0[3]); w.z = pk2(p1[0], p1[1]); w.w = pk2(p1[2], p1[3]);
;                     *(u32x4*)(base + (size_t)r * ldc + col0) = w; }
.LBB0_344:
	v_readlane_b32 s52, v254, 2
	v_readlane_b32 s54, v254, 4
	v_readlane_b32 s53, v254, 3
	v_readlane_b32 s55, v254, 5
	s_add_u32 s10, s54, s2
	s_addc_u32 s53, s55, s3
	s_lshl_b32 s2, s4, 8
	s_ashr_i32 s3, s2, 31
	s_lshl_b64 s[2:3], s[2:3], 2
	s_add_u32 s52, s10, s2
	v_ashrrev_i32_e32 v147, 4, v64
	s_addc_u32 s53, s53, s3
	v_and_or_b32 v144, v64, 15, s75
	s_cmp_lg_u32 s35, 0
	v_lshlrev_b32_e32 v146, 3, v147
	s_cbranch_scc0 .LBB0_353
	v_add_u32_e32 v148, s76, v146
	v_ashrrev_i32_e32 v149, 31, v148
	v_lshl_add_u64 v[76:77], v[148:149], 2, s[52:53]
	global_load_dwordx4 v[64:67], v[76:77], off offset:16
	global_load_dwordx4 v[72:75], v[76:77], off
	global_load_dwordx4 v[68:71], v[76:77], off offset:528
	s_nop 0
	global_load_dwordx4 v[76:79], v[76:77], off offset:512
	v_ashrrev_i32_e32 v145, 31, v144
	v_lshl_add_u64 v[150:151], v[144:145], 2, s[50:51]
	global_load_dword v152, v[150:151], off
	global_load_dword v216, v[150:151], off offset:64
	global_load_dword v218, v[150:151], off offset:128
	global_load_dword v220, v[150:151], off offset:192
	global_load_dword v222, v[150:151], off offset:512
	global_load_dword v224, v[150:151], off offset:576
	global_load_dword v226, v[150:151], off offset:640
	global_load_dword v228, v[150:151], off offset:704
	v_cvt_f32_i32_e32 v143, v143
	v_cvt_f32_i32_e32 v142, v142
	v_cvt_f32_i32_e32 v141, v141
	v_cvt_f32_i32_e32 v140, v140
	v_cvt_f32_i32_e32 v139, v139
	v_cvt_f32_i32_e32 v138, v138
	v_cvt_f32_i32_e32 v137, v137
	v_cvt_f32_i32_e32 v136, v136
	v_cvt_f32_i32_e32 v135, v135
	v_cvt_f32_i32_e32 v134, v134
	v_cvt_f32_i32_e32 v133, v133
	v_cvt_f32_i32_e32 v132, v132
	v_cvt_f32_i32_e32 v131, v131
	v_cvt_f32_i32_e32 v130, v130
	v_cvt_f32_i32_e32 v129, v129
	v_cvt_f32_i32_e32 v128, v128
	v_cvt_f32_i32_e32 v127, v127
	v_cvt_f32_i32_e32 v126, v126
	v_cvt_f32_i32_e32 v125, v125
	v_cvt_f32_i32_e32 v124, v124
	v_cvt_f32_i32_e32 v123, v123
	v_cvt_f32_i32_e32 v122, v122
	v_cvt_f32_i32_e32 v121, v121
	v_cvt_f32_i32_e32 v120, v120
	v_cvt_f32_i32_e32 v119, v119
	v_cvt_f32_i32_e32 v118, v118
	v_cvt_f32_i32_e32 v117, v117
	v_cvt_f32_i32_e32 v116, v116
	v_cvt_f32_i32_e32 v115, v115
	v_cvt_f32_i32_e32 v114, v114
	v_cvt_f32_i32_e32 v113, v113
	v_cvt_f32_i32_e32 v112, v112
	v_cvt_f32_i32_e32 v111, v111
	v_cvt_f32_i32_e32 v110, v110
	v_cvt_f32_i32_e32 v109, v109
	v_cvt_f32_i32_e32 v108, v108
	v_cvt_f32_i32_e32 v107, v107
	v_cvt_f32_i32_e32 v106, v106
	v_cvt_f32_i32_e32 v105, v105
	v_cvt_f32_i32_e32 v104, v104
	v_cvt_f32_i32_e32 v103, v103
	v_cvt_f32_i32_e32 v102, v102
	v_cvt_f32_i32_e32 v101, v101
	v_cvt_f32_i32_e32 v100, v100
	v_cvt_f32_i32_e32 v99, v99
	v_cvt_f32_i32_e32 v98, v98
	v_cvt_f32_i32_e32 v97, v97
	v_cvt_f32_i32_e32 v96, v96
	v_cvt_f32_i32_e32 v95, v95
	v_cvt_f32_i32_e32 v94, v94
	v_cvt_f32_i32_e32 v93, v93
	v_cvt_f32_i32_e32 v92, v92
	v_cvt_f32_i32_e32 v91, v91
	v_cvt_f32_i32_e32 v90, v90
	v_cvt_f32_i32_e32 v89, v89
	v_cvt_f32_i32_e32 v88, v88
	v_cvt_f32_i32_e32 v87, v87
	v_cvt_f32_i32_e32 v86, v86
	v_cvt_f32_i32_e32 v85, v85
	v_cvt_f32_i32_e32 v84, v84
	v_cvt_f32_i32_e32 v83, v83
	v_cvt_f32_i32_e32 v82, v82
	v_cvt_f32_i32_e32 v81, v81
	v_cvt_f32_i32_e32 v80, v80
	v_add_u32_e32 v176, 0x80, v144
	s_cmp_gt_i32 s83, 15
	v_lshl_add_u64 v[148:149], v[148:149], 1, s[44:45]
	s_mov_b64 s[2:3], -1
	v_mul_lo_u32 v178, v145, s35
	v_ashrrev_i32_e32 v177, 31, v176
	v_add_u32_e32 v175, 0x90, v144
	v_add_u32_e32 v174, 0xa0, v144
	v_add_u32_e32 v173, 0xb0, v144
	s_cbranch_scc1 .LBB0_347
	v_mad_u64_u32 v[180:181], s[2:3], v144, s35, 0
	v_mov_b32_e32 v182, v181
	v_mad_u64_u32 v[182:183], s[2:3], v145, s35, v[182:183]
	v_mov_b32_e32 v181, v182
	v_lshl_add_u64 v[184:185], v[180:181], 1, v[148:149]
	v_cvt_f32_i32_e32 v181, v63
	v_cvt_f32_i32_e32 v180, v62
	v_cvt_f32_i32_e32 v183, v61
	v_cvt_f32_i32_e32 v182, v60
	v_cvt_f32_i32_e32 v189, v57
	s_waitcnt vmcnt(0)
	v_pk_mul_f32 v[180:181], v[152:153], v[180:181] op_sel_hi:[0,1]
	v_pk_mul_f32 v[186:187], v[74:75], v[180:181]
	v_pk_mul_f32 v[182:183], v[152:153], v[182:183] op_sel_hi:[0,1]
	v_pk_mul_f32 v[180:181], v[72:73], v[182:183]
	v_cvt_f32_i32_e32 v183, v59
	v_cvt_f32_i32_e32 v182, v58
	v_cvt_f32_i32_e32 v188, v56
	v_cvt_pk_bf16_f32 v180, v180, v181
	v_cvt_pk_bf16_f32 v181, v186, v187
	v_pk_mul_f32 v[182:183], v[152:153], v[182:183] op_sel_hi:[0,1]
	v_pk_mul_f32 v[188:189], v[152:153], v[188:189] op_sel_hi:[0,1]
	v_pk_mul_f32 v[190:191], v[66:67], v[182:183]
	v_pk_mul_f32 v[182:183], v[64:65], v[188:189]
	v_pk_mul_f32 v[186:187], v[152:153], v[136:137] op_sel_hi:[0,1]
	v_cvt_pk_bf16_f32 v182, v182, v183
	v_cvt_pk_bf16_f32 v183, v190, v191
	global_store_dwordx4 v[184:185], v[180:183], off
	v_pk_mul_f32 v[188:189], v[152:153], v[138:139] op_sel_hi:[0,1]
	v_pk_mul_f32 v[188:189], v[70:71], v[188:189]
	v_pk_mul_f32 v[180:181], v[152:153], v[140:141] op_sel_hi:[0,1]
	v_pk_mul_f32 v[182:183], v[152:153], v[142:143] op_sel_hi:[0,1]
	v_pk_mul_f32 v[182:183], v[78:79], v[182:183]
	v_pk_mul_f32 v[180:181], v[76:77], v[180:181]
	v_pk_mul_f32 v[186:187], v[68:69], v[186:187]
	v_cvt_pk_bf16_f32 v180, v180, v181
	v_cvt_pk_bf16_f32 v181, v182, v183
	v_cvt_pk_bf16_f32 v182, v186, v187
	v_cvt_pk_bf16_f32 v183, v188, v189
	global_store_dwordx4 v[184:185], v[180:183], off offset:256
	v_or_b32_e32 v179, 16, v144
	s_nop 0
	v_mad_u64_u32 v[180:181], s[2:3], v179, s35, 0
	v_add_u32_e32 v181, v181, v178
	v_lshl_add_u64 v[186:187], v[180:181], 1, v[148:149]
	v_cvt_f32_i32_e32 v181, v55
	v_cvt_f32_i32_e32 v180, v54
	v_cvt_f32_i32_e32 v183, v53
	v_cvt_f32_i32_e32 v182, v52
	v_cvt_f32_i32_e32 v191, v49
	v_cvt_f32_i32_e32 v190, v48
	v_or_b32_e32 v179, 32, v144
	v_pk_mul_f32 v[182:183], v[216:217], v[182:183] op_sel_hi:[0,1]
; DI unsigned pk2(float a, float b) { f32x2 f = {a, b}; bf16x2_t h = __builtin_convertvector(f, bf16x2_t); return __builtin_bit_cast(unsigned, h); }
;     __device__ __forceinline__ void operator()(const f32x4 (&acc)[2][2][4][2], const Unit& u, int wr, int wc, int fr, int fq) const {
;     ...
; #pragma unroll
;         for (int ai = 0; ai < 2; ++ai)
; #pragma unroll
;             for (int m = 0; m < 4; ++m) { const int r = row0 + ai * HALF + m * 16; const float sr = sA[r]; bf16_t* rowp = base + (size_t)r * ldc + col0;
; #pragma unroll
;                 for (int bj = 0; bj < 2; ++bj) { const f32x4 v0 = __builtin_convertvector(__builtin_bit_cast(i32x4_t, acc[ai][bj][m][0]), f32x4) * sr * sb[bj][0], v1 = __builtin_convertvector(__builtin_bit_cast(i32x4_t, acc[ai][bj][m][1]), f32x4) * sr * sb[bj][1];
;                     u32x4 w; w.x = pk2(v0[0], v0[1]); w.y = pk2(v0[2], v0[3]); w.z = pk2(v1[0], v1[1]); w.w = pk2(v1[2], v1[3]);
;                     *(u32x4*)(rowp + bj * HALF) = w; } }
	v_pk_mul_f32 v[180:181], v[216:217], v[180:181] op_sel_hi:[0,1]
	v_pk_mul_f32 v[188:189], v[74:75], v[180:181]
	v_pk_mul_f32 v[180:181], v[72:73], v[182:183]
	v_cvt_f32_i32_e32 v183, v51
	v_cvt_f32_i32_e32 v182, v50
	v_pk_mul_f32 v[190:191], v[216:217], v[190:191] op_sel_hi:[0,1]
	v_cvt_pk_bf16_f32 v180, v180, v181
	v_cvt_pk_bf16_f32 v181, v188, v189
	v_pk_mul_f32 v[182:183], v[216:217], v[182:183] op_sel_hi:[0,1]
	v_pk_mul_f32 v[192:193], v[66:67], v[182:183]
	v_pk_mul_f32 v[182:183], v[64:65], v[190:191]
	v_pk_mul_f32 v[188:189], v[216:217], v[128:129] op_sel_hi:[0,1]
	v_cvt_pk_bf16_f32 v182, v182, v183
	v_cvt_pk_bf16_f32 v183, v192, v193
	global_store_dwordx4 v[186:187], v[180:183], off
	v_pk_mul_f32 v[188:189], v[68:69], v[188:189]
	v_cvt_f32_i32_e32 v191, v41
	v_pk_mul_f32 v[180:181], v[216:217], v[132:133] op_sel_hi:[0,1]
	v_pk_mul_f32 v[182:183], v[216:217], v[134:135] op_sel_hi:[0,1]
	v_pk_mul_f32 v[184:185], v[216:217], v[130:131] op_sel_hi:[0,1]
	v_pk_mul_f32 v[182:183], v[78:79], v[182:183]
	v_pk_mul_f32 v[180:181], v[76:77], v[180:181]
	v_pk_mul_f32 v[184:185], v[70:71], v[184:185]
	v_cvt_pk_bf16_f32 v180, v180, v181
	v_cvt_pk_bf16_f32 v181, v182, v183
	v_cvt_pk_bf16_f32 v182, v188, v189
	v_cvt_pk_bf16_f32 v183, v184, v185
	global_store_dwordx4 v[186:187], v[180:183], off offset:256
	v_cvt_f32_i32_e32 v190, v40
	s_nop 0
	v_mad_u64_u32 v[180:181], s[2:3], v179, s35, 0
	v_add_u32_e32 v181, v181, v178
	v_lshl_add_u64 v[186:187], v[180:181], 1, v[148:149]
	v_cvt_f32_i32_e32 v181, v47
	v_cvt_f32_i32_e32 v180, v46
	v_cvt_f32_i32_e32 v183, v45
	v_cvt_f32_i32_e32 v182, v44
	v_or_b32_e32 v179, 48, v144
	v_pk_mul_f32 v[182:183], v[218:219], v[182:183] op_sel_hi:[0,1]
	v_pk_mul_f32 v[180:181], v[218:219], v[180:181] op_sel_hi:[0,1]
	v_pk_mul_f32 v[188:189], v[74:75], v[180:181]
	v_pk_mul_f32 v[180:181], v[72:73], v[182:183]
	v_cvt_f32_i32_e32 v183, v43
	v_cvt_f32_i32_e32 v182, v42
	v_pk_mul_f32 v[190:191], v[218:219], v[190:191] op_sel_hi:[0,1]
	v_cvt_pk_bf16_f32 v180, v180, v181
	v_cvt_pk_bf16_f32 v181, v188, v189
	v_pk_mul_f32 v[182:183], v[218:219], v[182:183] op_sel_hi:[0,1]
	v_pk_mul_f32 v[192:193], v[66:67], v[182:183]
	v_pk_mul_f32 v[182:183], v[64:65], v[190:191]
	v_pk_mul_f32 v[188:189], v[218:219], v[120:121] op_sel_hi:[0,1]
	v_cvt_pk_bf16_f32 v182, v182, v183
	v_cvt_pk_bf16_f32 v183, v192, v193
	global_store_dwordx4 v[186:187], v[180:183], off
	v_pk_mul_f32 v[188:189], v[68:69], v[188:189]
	v_cvt_f32_i32_e32 v191, v33
	v_pk_mul_f32 v[180:181], v[218:219], v[124:125] op_sel_hi:[0,1]
	v_pk_mul_f32 v[182:183], v[218:219], v[126:127] op_sel_hi:[0,1]
	v_pk_mul_f32 v[184:185], v[218:219], v[122:123] op_sel_hi:[0,1]
	v_pk_mul_f32 v[182:183], v[78:79], v[182:183]
	v_pk_mul_f32 v[180:181], v[76:77], v[180:181]
	v_pk_mul_f32 v[184:185], v[70:71], v[184:185]
	v_cvt_pk_bf16_f32 v180, v180, v181
	v_cvt_pk_bf16_f32 v181, v182, v183
	v_cvt_pk_bf16_f32 v182, v188, v189
	v_cvt_pk_bf16_f32 v183, v184, v185
	global_store_dwordx4 v[186:187], v[180:183], off offset:256
	v_cvt_f32_i32_e32 v190, v32
	s_nop 0
	v_mad_u64_u32 v[180:181], s[2:3], v179, s35, 0
	v_add_u32_e32 v181, v181, v178
	v_lshl_add_u64 v[186:187], v[180:181], 1, v[148:149]
	v_cvt_f32_i32_e32 v181, v39
	v_cvt_f32_i32_e32 v180, v38
	v_cvt_f32_i32_e32 v183, v37
	v_cvt_f32_i32_e32 v182, v36
	v_ashrrev_i32_e32 v179, 31, v175
	v_pk_mul_f32 v[182:183], v[220:221], v[182:183] op_sel_hi:[0,1]
	v_pk_mul_f32 v[180:181], v[220:221], v[180:181] op_sel_hi:[0,1]
	v_pk_mul_f32 v[188:189], v[74:75], v[180:181]
	v_pk_mul_f32 v[180:181], v[72:73], v[182:183]
	v_cvt_f32_i32_e32 v183, v35
	v_cvt_f32_i32_e32 v182, v34
	v_pk_mul_f32 v[190:191], v[220:221], v[190:191] op_sel_hi:[0,1]
	v_cvt_pk_bf16_f32 v180, v180, v181
	v_cvt_pk_bf16_f32 v181, v188, v189
	v_pk_mul_f32 v[182:183], v[220:221], v[182:183] op_sel_hi:[0,1]
	v_pk_mul_f32 v[192:193], v[66:67], v[182:183]
	v_pk_mul_f32 v[182:183], v[64:65], v[190:191]
	v_pk_mul_f32 v[188:189], v[220:221], v[112:113] op_sel_hi:[0,1]
	v_cvt_pk_bf16_f32 v182, v182, v183
	v_cvt_pk_bf16_f32 v183, v192, v193
	global_store_dwordx4 v[186:187], v[180:183], off
	v_pk_mul_f32 v[188:189], v[68:69], v[188:189]
	v_cvt_f32_i32_e32 v191, v25
	v_pk_mul_f32 v[180:181], v[220:221], v[116:117] op_sel_hi:[0,1]
	v_pk_mul_f32 v[182:183], v[220:221], v[118:119] op_sel_hi:[0,1]
	v_pk_mul_f32 v[184:185], v[220:221], v[114:115] op_sel_hi:[0,1]
	v_pk_mul_f32 v[182:183], v[78:79], v[182:183]
	v_pk_mul_f32 v[180:181], v[76:77], v[180:181]
	v_pk_mul_f32 v[184:185], v[70:71], v[184:185]
	v_cvt_pk_bf16_f32 v180, v180, v181
	v_cvt_pk_bf16_f32 v181, v182, v183
	v_cvt_pk_bf16_f32 v182, v188, v189
	v_cvt_pk_bf16_f32 v183, v184, v185
	global_store_dwordx4 v[186:187], v[180:183], off offset:256
	v_cvt_f32_i32_e32 v190, v24
	s_nop 0
	v_mad_u64_u32 v[180:181], s[2:3], v176, s35, 0
	v_mov_b32_e32 v182, v181
	v_mad_u64_u32 v[182:183], s[2:3], v177, s35, v[182:183]
	v_mov_b32_e32 v181, v182
	v_lshl_add_u64 v[186:187], v[180:181], 1, v[148:149]
	v_cvt_f32_i32_e32 v181, v31
	v_cvt_f32_i32_e32 v180, v30
	v_cvt_f32_i32_e32 v183, v29
	v_cvt_f32_i32_e32 v182, v28
	v_pk_mul_f32 v[182:183], v[222:223], v[182:183] op_sel_hi:[0,1]
	v_pk_mul_f32 v[180:181], v[222:223], v[180:181] op_sel_hi:[0,1]
	v_pk_mul_f32 v[188:189], v[74:75], v[180:181]
	v_pk_mul_f32 v[180:181], v[72:73], v[182:183]
	v_cvt_f32_i32_e32 v183, v27
	v_cvt_f32_i32_e32 v182, v26
	v_pk_mul_f32 v[190:191], v[222:223], v[190:191] op_sel_hi:[0,1]
	v_cvt_pk_bf16_f32 v180, v180, v181
	v_cvt_pk_bf16_f32 v181, v188, v189
	v_pk_mul_f32 v[182:183], v[222:223], v[182:183] op_sel_hi:[0,1]
	v_pk_mul_f32 v[192:193], v[66:67], v[182:183]
	v_pk_mul_f32 v[182:183], v[64:65], v[190:191]
; DI unsigned pk2(float a, float b) { f32x2 f = {a, b}; bf16x2_t h = __builtin_convertvector(f, bf16x2_t); return __builtin_bit_cast(unsigned, h); }
;     __device__ __forceinline__ void operator()(const f32x4 (&acc)[2][2][4][2], const Unit& u, int wr, int wc, int fr, int fq) const {
;     ...
; #pragma unroll
;         for (int ai = 0; ai < 2; ++ai)
; #pragma unroll
;             for (int m = 0; m < 4; ++m) { const int r = row0 + ai * HALF + m * 16; const float sr = sA[r]; bf16_t* rowp = base + (size_t)r * ldc + col0;
; #pragma unroll
;                 for (int bj = 0; bj < 2; ++bj) { const f32x4 v0 = __builtin_convertvector(__builtin_bit_cast(i32x4_t, acc[ai][bj][m][0]), f32x4) * sr * sb[bj][0], v1 = __builtin_convertvector(__builtin_bit_cast(i32x4_t, acc[ai][bj][m][1]), f32x4) * sr * sb[bj][1];
;                     u32x4 w; w.x = pk2(v0[0], v0[1]); w.y = pk2(v0[2], v0[3]); w.z = pk2(v1[0], v1[1]); w.w = pk2(v1[2], v1[3]);
;                     *(u32x4*)(rowp + bj * HALF) = w; } }
	v_pk_mul_f32 v[188:189], v[222:223], v[104:105] op_sel_hi:[0,1]
	v_cvt_pk_bf16_f32 v182, v182, v183
	v_cvt_pk_bf16_f32 v183, v192, v193
	global_store_dwordx4 v[186:187], v[180:183], off
	v_pk_mul_f32 v[188:189], v[68:69], v[188:189]
	v_cvt_f32_i32_e32 v191, v17
	v_pk_mul_f32 v[180:181], v[222:223], v[108:109] op_sel_hi:[0,1]
	v_pk_mul_f32 v[182:183], v[222:223], v[110:111] op_sel_hi:[0,1]
	v_pk_mul_f32 v[184:185], v[222:223], v[106:107] op_sel_hi:[0,1]
	v_pk_mul_f32 v[182:183], v[78:79], v[182:183]
	v_pk_mul_f32 v[180:181], v[76:77], v[180:181]
	v_pk_mul_f32 v[184:185], v[70:71], v[184:185]
	v_cvt_pk_bf16_f32 v180, v180, v181
	v_cvt_pk_bf16_f32 v181, v182, v183
	v_cvt_pk_bf16_f32 v182, v188, v189
	v_cvt_pk_bf16_f32 v183, v184, v185
	global_store_dwordx4 v[186:187], v[180:183], off offset:256
	v_cvt_f32_i32_e32 v190, v16
	s_nop 0
	v_mad_u64_u32 v[180:181], s[2:3], v175, s35, 0
	v_mov_b32_e32 v182, v181
	v_mad_u64_u32 v[182:183], s[2:3], v179, s35, v[182:183]
	v_mov_b32_e32 v181, v182
	v_lshl_add_u64 v[186:187], v[180:181], 1, v[148:149]
	v_cvt_f32_i32_e32 v181, v23
	v_cvt_f32_i32_e32 v180, v22
	v_cvt_f32_i32_e32 v183, v21
	v_cvt_f32_i32_e32 v182, v20
	v_ashrrev_i32_e32 v179, 31, v174
	v_pk_mul_f32 v[182:183], v[224:225], v[182:183] op_sel_hi:[0,1]
	v_pk_mul_f32 v[180:181], v[224:225], v[180:181] op_sel_hi:[0,1]
	v_pk_mul_f32 v[188:189], v[74:75], v[180:181]
	v_pk_mul_f32 v[180:181], v[72:73], v[182:183]
	v_cvt_f32_i32_e32 v183, v19
	v_cvt_f32_i32_e32 v182, v18
	v_pk_mul_f32 v[190:191], v[224:225], v[190:191] op_sel_hi:[0,1]
	v_cvt_pk_bf16_f32 v180, v180, v181
	v_cvt_pk_bf16_f32 v181, v188, v189
	v_pk_mul_f32 v[182:183], v[224:225], v[182:183] op_sel_hi:[0,1]
	v_pk_mul_f32 v[192:193], v[66:67], v[182:183]
	v_pk_mul_f32 v[182:183], v[64:65], v[190:191]
	v_pk_mul_f32 v[188:189], v[224:225], v[96:97] op_sel_hi:[0,1]
	v_cvt_pk_bf16_f32 v182, v182, v183
	v_cvt_pk_bf16_f32 v183, v192, v193
	global_store_dwordx4 v[186:187], v[180:183], off
	v_pk_mul_f32 v[188:189], v[68:69], v[188:189]
	v_cvt_f32_i32_e32 v191, v9
	v_pk_mul_f32 v[180:181], v[224:225], v[100:101] op_sel_hi:[0,1]
	v_pk_mul_f32 v[182:183], v[224:225], v[102:103] op_sel_hi:[0,1]
	v_pk_mul_f32 v[184:185], v[224:225], v[98:99] op_sel_hi:[0,1]
	v_pk_mul_f32 v[182:183], v[78:79], v[182:183]
	v_pk_mul_f32 v[180:181], v[76:77], v[180:181]
	v_pk_mul_f32 v[184:185], v[70:71], v[184:185]
	v_cvt_pk_bf16_f32 v180, v180, v181
	v_cvt_pk_bf16_f32 v181, v182, v183
	v_cvt_pk_bf16_f32 v182, v188, v189
	v_cvt_pk_bf16_f32 v183, v184, v185
	global_store_dwordx4 v[186:187], v[180:183], off offset:256
	v_cvt_f32_i32_e32 v190, v8
	s_nop 0
	v_mad_u64_u32 v[180:181], s[2:3], v174, s35, 0
	v_mov_b32_e32 v182, v181
	v_mad_u64_u32 v[182:183], s[2:3], v179, s35, v[182:183]
	v_mov_b32_e32 v181, v182
	v_lshl_add_u64 v[186:187], v[180:181], 1, v[148:149]
	v_cvt_f32_i32_e32 v181, v15
	v_cvt_f32_i32_e32 v180, v14
	v_cvt_f32_i32_e32 v183, v13
	v_cvt_f32_i32_e32 v182, v12
	v_ashrrev_i32_e32 v179, 31, v173
	v_pk_mul_f32 v[182:183], v[226:227], v[182:183] op_sel_hi:[0,1]
	v_pk_mul_f32 v[180:181], v[226:227], v[180:181] op_sel_hi:[0,1]
	v_pk_mul_f32 v[188:189], v[74:75], v[180:181]
	v_pk_mul_f32 v[180:181], v[72:73], v[182:183]
	v_cvt_f32_i32_e32 v183, v11
	v_cvt_f32_i32_e32 v182, v10
	v_pk_mul_f32 v[190:191], v[226:227], v[190:191] op_sel_hi:[0,1]
	v_cvt_pk_bf16_f32 v180, v180, v181
	v_cvt_pk_bf16_f32 v181, v188, v189
	v_pk_mul_f32 v[182:183], v[226:227], v[182:183] op_sel_hi:[0,1]
	v_pk_mul_f32 v[192:193], v[66:67], v[182:183]
	v_pk_mul_f32 v[182:183], v[64:65], v[190:191]
	v_pk_mul_f32 v[188:189], v[226:227], v[88:89] op_sel_hi:[0,1]
	v_cvt_pk_bf16_f32 v182, v182, v183
	v_cvt_pk_bf16_f32 v183, v192, v193
	global_store_dwordx4 v[186:187], v[180:183], off
	v_pk_mul_f32 v[188:189], v[68:69], v[188:189]
	v_cvt_f32_i32_e32 v191, v1
	v_pk_mul_f32 v[180:181], v[226:227], v[92:93] op_sel_hi:[0,1]
	v_pk_mul_f32 v[182:183], v[226:227], v[94:95] op_sel_hi:[0,1]
	v_pk_mul_f32 v[184:185], v[226:227], v[90:91] op_sel_hi:[0,1]
	v_pk_mul_f32 v[182:183], v[78:79], v[182:183]
	v_pk_mul_f32 v[180:181], v[76:77], v[180:181]
	v_pk_mul_f32 v[184:185], v[70:71], v[184:185]
	v_cvt_pk_bf16_f32 v180, v180, v181
	v_cvt_pk_bf16_f32 v181, v182, v183
	v_cvt_pk_bf16_f32 v182, v188, v189
	v_cvt_pk_bf16_f32 v183, v184, v185
	global_store_dwordx4 v[186:187], v[180:183], off offset:256
	v_cvt_f32_i32_e32 v190, v0
	s_nop 0
	v_mad_u64_u32 v[180:181], s[2:3], v173, s35, 0
	v_mov_b32_e32 v182, v181
	v_mad_u64_u32 v[182:183], s[2:3], v179, s35, v[182:183]
	v_mov_b32_e32 v181, v182
	v_lshl_add_u64 v[186:187], v[180:181], 1, v[148:149]
	v_cvt_f32_i32_e32 v181, v7
	v_cvt_f32_i32_e32 v180, v6
	v_cvt_f32_i32_e32 v183, v5
	v_cvt_f32_i32_e32 v182, v4
	s_mov_b64 s[2:3], 0
	v_pk_mul_f32 v[182:183], v[228:229], v[182:183] op_sel_hi:[0,1]
	v_pk_mul_f32 v[180:181], v[228:229], v[180:181] op_sel_hi:[0,1]
	v_pk_mul_f32 v[188:189], v[74:75], v[180:181]
	v_pk_mul_f32 v[180:181], v[72:73], v[182:183]
	v_cvt_f32_i32_e32 v183, v3
	v_cvt_f32_i32_e32 v182, v2
	v_pk_mul_f32 v[190:191], v[228:229], v[190:191] op_sel_hi:[0,1]
	v_cvt_pk_bf16_f32 v180, v180, v181
	v_cvt_pk_bf16_f32 v181, v188, v189
	v_pk_mul_f32 v[182:183], v[228:229], v[182:183] op_sel_hi:[0,1]
	v_pk_mul_f32 v[192:193], v[66:67], v[182:183]
	v_pk_mul_f32 v[182:183], v[64:65], v[190:191]
	v_pk_mul_f32 v[188:189], v[228:229], v[80:81] op_sel_hi:[0,1]
	v_cvt_pk_bf16_f32 v182, v182, v183
	v_cvt_pk_bf16_f32 v183, v192, v193
	global_store_dwordx4 v[186:187], v[180:183], off
	v_pk_mul_f32 v[188:189], v[68:69], v[188:189]
	s_nop 0
	v_pk_mul_f32 v[180:181], v[228:229], v[84:85] op_sel_hi:[0,1]
	v_pk_mul_f32 v[182:183], v[228:229], v[86:87] op_sel_hi:[0,1]
	v_pk_mul_f32 v[184:185], v[228:229], v[82:83] op_sel_hi:[0,1]
	v_pk_mul_f32 v[182:183], v[78:79], v[182:183]
	v_pk_mul_f32 v[180:181], v[76:77], v[180:181]
	v_pk_mul_f32 v[184:185], v[70:71], v[184:185]
	v_cvt_pk_bf16_f32 v180, v180, v181
	v_cvt_pk_bf16_f32 v181, v182, v183
	v_cvt_pk_bf16_f32 v182, v188, v189
	v_cvt_pk_bf16_f32 v183, v184, v185
	global_store_dwordx4 v[186:187], v[180:183], off offset:256
; DI unsigned pk2(float a, float b) { f32x2 f = {a, b}; bf16x2_t h = __builtin_convertvector(f, bf16x2_t); return __builtin_bit_cast(unsigned, h); }
;     __device__ __forceinline__ void operator()(const f32x4 (&acc)[2][2][4][2], const Unit& u, int wr, int wc, int fr, int fq) const {
;     ...
;         if (u.a1 >= 16) {
; #pragma unroll
;             for (int ai = 0; ai < 2; ++ai)
; #pragma unroll
;                 for (int m = 0; m < 4; ++m) { const int r = row0 + ai * HALF + m * 16; const float sr = sA[r];
;                     const f32x4 p0 = (__builtin_convertvector(__builtin_bit_cast(i32x4_t, acc[ai][0][m][0]), f32x4) * sr * sb[0][0]) * (__builtin_convertvector(__builtin_bit_cast(i32x4_t, acc[ai][1][m][0]), f32x4) * sr * sb[1][0]);
;                     const f32x4 p1 = (__builtin_convertvector(__builtin_bit_cast(i32x4_t, acc[ai][0][m][1]), f32x4) * sr * sb[0][1]) * (__builtin_convertvector(__builtin_bit_cast(i32x4_t, acc[ai][1][m][1]), f32x4) * sr * sb[1][1]);
;                     u32x4 w; w.x = pk2(p0[0], p0[1]); w.y = pk2(p0[2], p0[3]); w.z = pk2(p1[0], p1[1]); w.w = pk2(p1[2], p1[3]);
;                     *(u32x4*)(base + (size_t)r * ldc + col0) = w; }
;             return; }
.LBB0_347:
	s_andn2_b64 vcc, exec, s[2:3]
	s_cbranch_vccnz .LBB0_349
	v_cvt_f32_i32_e32 v181, v61
	v_cvt_f32_i32_e32 v180, v60
	v_cvt_f32_i32_e32 v183, v63
	v_cvt_f32_i32_e32 v182, v62
	s_waitcnt vmcnt(0)
	v_pk_mul_f32 v[142:143], v[152:153], v[142:143] op_sel_hi:[0,1]
	v_pk_mul_f32 v[180:181], v[152:153], v[180:181] op_sel_hi:[0,1]
	v_pk_mul_f32 v[140:141], v[152:153], v[140:141] op_sel_hi:[0,1]
	v_pk_mul_f32 v[182:183], v[152:153], v[182:183] op_sel_hi:[0,1]
	v_pk_mul_f32 v[180:181], v[72:73], v[180:181]
	v_pk_mul_f32 v[182:183], v[74:75], v[182:183]
	v_pk_mul_f32 v[140:141], v[76:77], v[140:141]
	v_pk_mul_f32 v[142:143], v[78:79], v[142:143]
	v_pk_mul_f32 v[140:141], v[180:181], v[140:141]
	v_pk_mul_f32 v[142:143], v[182:183], v[142:143]
	v_cvt_f32_i32_e32 v181, v57
	v_cvt_f32_i32_e32 v180, v56
	v_cvt_f32_i32_e32 v183, v59
	v_cvt_f32_i32_e32 v182, v58
	v_pk_mul_f32 v[138:139], v[152:153], v[138:139] op_sel_hi:[0,1]
	v_pk_mul_f32 v[180:181], v[152:153], v[180:181] op_sel_hi:[0,1]
	v_pk_mul_f32 v[136:137], v[152:153], v[136:137] op_sel_hi:[0,1]
	v_pk_mul_f32 v[182:183], v[152:153], v[182:183] op_sel_hi:[0,1]
	v_pk_mul_f32 v[180:181], v[64:65], v[180:181]
	v_pk_mul_f32 v[182:183], v[66:67], v[182:183]
	v_pk_mul_f32 v[136:137], v[68:69], v[136:137]
	v_pk_mul_f32 v[138:139], v[70:71], v[138:139]
	s_nop 0
	v_pk_mul_f32 v[182:183], v[182:183], v[138:139]
	v_pk_mul_f32 v[138:139], v[180:181], v[136:137]
	v_cvt_pk_bf16_f32 v136, v140, v141
	v_mad_u64_u32 v[140:141], s[2:3], v144, s35, 0
	v_cvt_pk_bf16_f32 v137, v142, v143
	v_mov_b32_e32 v142, v141
	v_mad_u64_u32 v[142:143], s[2:3], v145, s35, v[142:143]
	v_mov_b32_e32 v141, v142
	v_cvt_pk_bf16_f32 v138, v138, v139
	v_cvt_pk_bf16_f32 v139, v182, v183
	v_lshl_add_u64 v[140:141], v[140:141], 1, v[148:149]
	global_store_dwordx4 v[140:141], v[136:139], off
	v_cvt_f32_i32_e32 v141, v55
	s_nop 0
	v_cvt_f32_i32_e32 v139, v53
	v_cvt_f32_i32_e32 v138, v52
	v_cvt_f32_i32_e32 v140, v54
	v_or_b32_e32 v142, 16, v144
	v_pk_mul_f32 v[140:141], v[216:217], v[140:141] op_sel_hi:[0,1]
	v_pk_mul_f32 v[138:139], v[216:217], v[138:139] op_sel_hi:[0,1]
	v_pk_mul_f32 v[134:135], v[216:217], v[134:135] op_sel_hi:[0,1]
	v_pk_mul_f32 v[132:133], v[216:217], v[132:133] op_sel_hi:[0,1]
	v_pk_mul_f32 v[138:139], v[72:73], v[138:139]
	v_pk_mul_f32 v[140:141], v[74:75], v[140:141]
	v_pk_mul_f32 v[132:133], v[76:77], v[132:133]
	v_pk_mul_f32 v[134:135], v[78:79], v[134:135]
	v_pk_mul_f32 v[132:133], v[138:139], v[132:133]
	v_pk_mul_f32 v[134:135], v[140:141], v[134:135]
	v_cvt_f32_i32_e32 v139, v49
	v_cvt_f32_i32_e32 v138, v48
	v_cvt_f32_i32_e32 v141, v51
	v_cvt_f32_i32_e32 v140, v50
	v_pk_mul_f32 v[130:131], v[216:217], v[130:131] op_sel_hi:[0,1]
	v_pk_mul_f32 v[138:139], v[216:217], v[138:139] op_sel_hi:[0,1]
	v_pk_mul_f32 v[128:129], v[216:217], v[128:129] op_sel_hi:[0,1]
	v_pk_mul_f32 v[140:141], v[216:217], v[140:141] op_sel_hi:[0,1]
	v_pk_mul_f32 v[138:139], v[64:65], v[138:139]
	v_pk_mul_f32 v[140:141], v[66:67], v[140:141]
	v_pk_mul_f32 v[128:129], v[68:69], v[128:129]
	v_pk_mul_f32 v[130:131], v[70:71], v[130:131]
	s_nop 0
	v_pk_mul_f32 v[136:137], v[140:141], v[130:131]
	v_pk_mul_f32 v[130:131], v[138:139], v[128:129]
	v_cvt_pk_bf16_f32 v128, v132, v133
	v_mad_u64_u32 v[132:133], s[2:3], v142, s35, 0
	v_add_u32_e32 v133, v133, v178
	v_cvt_pk_bf16_f32 v129, v134, v135
	v_cvt_pk_bf16_f32 v130, v130, v131
	v_cvt_pk_bf16_f32 v131, v136, v137
	v_lshl_add_u64 v[132:133], v[132:133], 1, v[148:149]
	global_store_dwordx4 v[132:133], v[128:131], off
	v_cvt_f32_i32_e32 v133, v47
	s_nop 0
	v_cvt_f32_i32_e32 v131, v45
	v_cvt_f32_i32_e32 v130, v44
	v_cvt_f32_i32_e32 v132, v46
	v_or_b32_e32 v134, 32, v144
	v_pk_mul_f32 v[132:133], v[218:219], v[132:133] op_sel_hi:[0,1]
	v_pk_mul_f32 v[130:131], v[218:219], v[130:131] op_sel_hi:[0,1]
	v_pk_mul_f32 v[126:127], v[218:219], v[126:127] op_sel_hi:[0,1]
	v_pk_mul_f32 v[124:125], v[218:219], v[124:125] op_sel_hi:[0,1]
	v_pk_mul_f32 v[130:131], v[72:73], v[130:131]
	v_pk_mul_f32 v[132:133], v[74:75], v[132:133]
	v_pk_mul_f32 v[124:125], v[76:77], v[124:125]
	v_pk_mul_f32 v[126:127], v[78:79], v[126:127]
	v_pk_mul_f32 v[124:125], v[130:131], v[124:125]
	v_pk_mul_f32 v[126:127], v[132:133], v[126:127]
	v_cvt_f32_i32_e32 v131, v41
	v_cvt_f32_i32_e32 v130, v40
	v_cvt_f32_i32_e32 v133, v43
	v_cvt_f32_i32_e32 v132, v42
	v_pk_mul_f32 v[122:123], v[218:219], v[122:123] op_sel_hi:[0,1]
	v_pk_mul_f32 v[130:131], v[218:219], v[130:131] op_sel_hi:[0,1]
	v_pk_mul_f32 v[120:121], v[218:219], v[120:121] op_sel_hi:[0,1]
	v_pk_mul_f32 v[132:133], v[218:219], v[132:133] op_sel_hi:[0,1]
	v_pk_mul_f32 v[130:131], v[64:65], v[130:131]
	v_pk_mul_f32 v[132:133], v[66:67], v[132:133]
	v_pk_mul_f32 v[120:121], v[68:69], v[120:121]
	v_pk_mul_f32 v[122:123], v[70:71], v[122:123]
	s_nop 0
	v_pk_mul_f32 v[128:129], v[132:133], v[122:123]
	v_pk_mul_f32 v[122:123], v[130:131], v[120:121]
	v_cvt_pk_bf16_f32 v120, v124, v125
	v_mad_u64_u32 v[124:125], s[2:3], v134, s35, 0
	v_add_u32_e32 v125, v125, v178
	v_cvt_pk_bf16_f32 v121, v126, v127
	v_cvt_pk_bf16_f32 v122, v122, v123
	v_cvt_pk_bf16_f32 v123, v128, v129
	v_lshl_add_u64 v[124:125], v[124:125], 1, v[148:149]
	global_store_dwordx4 v[124:125], v[120:123], off
	v_cvt_f32_i32_e32 v125, v39
	s_nop 0
	v_cvt_f32_i32_e32 v123, v37
	v_cvt_f32_i32_e32 v122, v36
	v_cvt_f32_i32_e32 v124, v38
	v_or_b32_e32 v126, 48, v144
	v_pk_mul_f32 v[124:125], v[220:221], v[124:125] op_sel_hi:[0,1]
	v_pk_mul_f32 v[122:123], v[220:221], v[122:123] op_sel_hi:[0,1]
	v_pk_mul_f32 v[118:119], v[220:221], v[118:119] op_sel_hi:[0,1]
	v_pk_mul_f32 v[116:117], v[220:221], v[116:117] op_sel_hi:[0,1]
; DI unsigned pk2(float a, float b) { f32x2 f = {a, b}; bf16x2_t h = __builtin_convertvector(f, bf16x2_t); return __builtin_bit_cast(unsigned, h); }
;     __device__ __forceinline__ void operator()(const f32x4 (&acc)[2][2][4][2], const Unit& u, int wr, int wc, int fr, int fq) const {
;     ...
;         if (u.a1 >= 16) {
; #pragma unroll
;             for (int ai = 0; ai < 2; ++ai)
; #pragma unroll
;                 for (int m = 0; m < 4; ++m) { const int r = row0 + ai * HALF + m * 16; const float sr = sA[r];
;                     const f32x4 p0 = (__builtin_convertvector(__builtin_bit_cast(i32x4_t, acc[ai][0][m][0]), f32x4) * sr * sb[0][0]) * (__builtin_convertvector(__builtin_bit_cast(i32x4_t, acc[ai][1][m][0]), f32x4) * sr * sb[1][0]);
;                     const f32x4 p1 = (__builtin_convertvector(__builtin_bit_cast(i32x4_t, acc[ai][0][m][1]), f32x4) * sr * sb[0][1]) * (__builtin_convertvector(__builtin_bit_cast(i32x4_t, acc[ai][1][m][1]), f32x4) * sr * sb[1][1]);
;                     u32x4 w; w.x = pk2(p0[0], p0[1]); w.y = pk2(p0[2], p0[3]); w.z = pk2(p1[0], p1[1]); w.w = pk2(p1[2], p1[3]);
;                     *(u32x4*)(base + (size_t)r * ldc + col0) = w; }
;             return; }
	v_pk_mul_f32 v[122:123], v[72:73], v[122:123]
	v_pk_mul_f32 v[124:125], v[74:75], v[124:125]
	v_pk_mul_f32 v[116:117], v[76:77], v[116:117]
	v_pk_mul_f32 v[118:119], v[78:79], v[118:119]
	v_pk_mul_f32 v[116:117], v[122:123], v[116:117]
	v_pk_mul_f32 v[118:119], v[124:125], v[118:119]
	v_cvt_f32_i32_e32 v123, v33
	v_cvt_f32_i32_e32 v122, v32
	v_cvt_f32_i32_e32 v125, v35
	v_cvt_f32_i32_e32 v124, v34
	v_pk_mul_f32 v[114:115], v[220:221], v[114:115] op_sel_hi:[0,1]
	v_pk_mul_f32 v[122:123], v[220:221], v[122:123] op_sel_hi:[0,1]
	v_pk_mul_f32 v[112:113], v[220:221], v[112:113] op_sel_hi:[0,1]
	v_pk_mul_f32 v[124:125], v[220:221], v[124:125] op_sel_hi:[0,1]
	v_pk_mul_f32 v[122:123], v[64:65], v[122:123]
	v_pk_mul_f32 v[124:125], v[66:67], v[124:125]
	v_pk_mul_f32 v[112:113], v[68:69], v[112:113]
	v_pk_mul_f32 v[114:115], v[70:71], v[114:115]
	s_nop 0
	v_pk_mul_f32 v[120:121], v[124:125], v[114:115]
	v_pk_mul_f32 v[114:115], v[122:123], v[112:113]
	v_cvt_pk_bf16_f32 v112, v116, v117
	v_mad_u64_u32 v[116:117], s[2:3], v126, s35, 0
	v_add_u32_e32 v117, v117, v178
	v_cvt_pk_bf16_f32 v113, v118, v119
	v_cvt_pk_bf16_f32 v114, v114, v115
	v_cvt_pk_bf16_f32 v115, v120, v121
	v_lshl_add_u64 v[116:117], v[116:117], 1, v[148:149]
	global_store_dwordx4 v[116:117], v[112:115], off
	v_cvt_f32_i32_e32 v117, v31
	s_nop 0
	v_cvt_f32_i32_e32 v115, v29
	v_cvt_f32_i32_e32 v114, v28
	v_cvt_f32_i32_e32 v116, v30
	v_pk_mul_f32 v[116:117], v[222:223], v[116:117] op_sel_hi:[0,1]
	v_pk_mul_f32 v[114:115], v[222:223], v[114:115] op_sel_hi:[0,1]
	v_pk_mul_f32 v[110:111], v[222:223], v[110:111] op_sel_hi:[0,1]
	v_pk_mul_f32 v[108:109], v[222:223], v[108:109] op_sel_hi:[0,1]
	v_pk_mul_f32 v[114:115], v[72:73], v[114:115]
	v_pk_mul_f32 v[116:117], v[74:75], v[116:117]
	v_pk_mul_f32 v[108:109], v[76:77], v[108:109]
	v_pk_mul_f32 v[110:111], v[78:79], v[110:111]
	v_pk_mul_f32 v[108:109], v[114:115], v[108:109]
	v_pk_mul_f32 v[110:111], v[116:117], v[110:111]
	v_cvt_f32_i32_e32 v115, v25
	v_cvt_f32_i32_e32 v114, v24
	v_cvt_f32_i32_e32 v117, v27
	v_cvt_f32_i32_e32 v116, v26
	v_pk_mul_f32 v[106:107], v[222:223], v[106:107] op_sel_hi:[0,1]
	v_pk_mul_f32 v[114:115], v[222:223], v[114:115] op_sel_hi:[0,1]
	v_pk_mul_f32 v[104:105], v[222:223], v[104:105] op_sel_hi:[0,1]
	v_pk_mul_f32 v[116:117], v[222:223], v[116:117] op_sel_hi:[0,1]
	v_pk_mul_f32 v[114:115], v[64:65], v[114:115]
	v_pk_mul_f32 v[116:117], v[66:67], v[116:117]
	v_pk_mul_f32 v[104:105], v[68:69], v[104:105]
	v_pk_mul_f32 v[106:107], v[70:71], v[106:107]
	s_nop 0
	v_pk_mul_f32 v[112:113], v[116:117], v[106:107]
	v_pk_mul_f32 v[106:107], v[114:115], v[104:105]
	v_cvt_pk_bf16_f32 v104, v108, v109
	v_mad_u64_u32 v[108:109], s[2:3], v176, s35, 0
	v_cvt_pk_bf16_f32 v105, v110, v111
	v_mov_b32_e32 v110, v109
	v_mad_u64_u32 v[110:111], s[2:3], v177, s35, v[110:111]
	v_mov_b32_e32 v109, v110
	v_cvt_pk_bf16_f32 v106, v106, v107
	v_cvt_pk_bf16_f32 v107, v112, v113
	v_lshl_add_u64 v[108:109], v[108:109], 1, v[148:149]
	global_store_dwordx4 v[108:109], v[104:107], off
	v_cvt_f32_i32_e32 v109, v23
	s_nop 0
	v_cvt_f32_i32_e32 v107, v21
	v_cvt_f32_i32_e32 v106, v20
	v_cvt_f32_i32_e32 v108, v22
	v_ashrrev_i32_e32 v110, 31, v175
	v_pk_mul_f32 v[108:109], v[224:225], v[108:109] op_sel_hi:[0,1]
	v_pk_mul_f32 v[106:107], v[224:225], v[106:107] op_sel_hi:[0,1]
	v_pk_mul_f32 v[102:103], v[224:225], v[102:103] op_sel_hi:[0,1]
	v_pk_mul_f32 v[100:101], v[224:225], v[100:101] op_sel_hi:[0,1]
	v_pk_mul_f32 v[106:107], v[72:73], v[106:107]
	v_pk_mul_f32 v[108:109], v[74:75], v[108:109]
	v_pk_mul_f32 v[100:101], v[76:77], v[100:101]
	v_pk_mul_f32 v[102:103], v[78:79], v[102:103]
	v_pk_mul_f32 v[100:101], v[106:107], v[100:101]
	v_pk_mul_f32 v[102:103], v[108:109], v[102:103]
	v_cvt_f32_i32_e32 v107, v17
	v_cvt_f32_i32_e32 v106, v16
	v_cvt_f32_i32_e32 v109, v19
	v_cvt_f32_i32_e32 v108, v18
	v_pk_mul_f32 v[98:99], v[224:225], v[98:99] op_sel_hi:[0,1]
	v_pk_mul_f32 v[106:107], v[224:225], v[106:107] op_sel_hi:[0,1]
	v_pk_mul_f32 v[96:97], v[224:225], v[96:97] op_sel_hi:[0,1]
; DI unsigned pk2(float a, float b) { f32x2 f = {a, b}; bf16x2_t h = __builtin_convertvector(f, bf16x2_t); return __builtin_bit_cast(unsigned, h); }
;     __device__ __forceinline__ void operator()(const f32x4 (&acc)[2][2][4][2], const Unit& u, int wr, int wc, int fr, int fq) const {
;     ...
;         if (u.a1 >= 16) {
; #pragma unroll
;             for (int ai = 0; ai < 2; ++ai)
; #pragma unroll
;                 for (int m = 0; m < 4; ++m) { const int r = row0 + ai * HALF + m * 16; const float sr = sA[r];
;                     const f32x4 p0 = (__builtin_convertvector(__builtin_bit_cast(i32x4_t, acc[ai][0][m][0]), f32x4) * sr * sb[0][0]) * (__builtin_convertvector(__builtin_bit_cast(i32x4_t, acc[ai][1][m][0]), f32x4) * sr * sb[1][0]);
;                     const f32x4 p1 = (__builtin_convertvector(__builtin_bit_cast(i32x4_t, acc[ai][0][m][1]), f32x4) * sr * sb[0][1]) * (__builtin_convertvector(__builtin_bit_cast(i32x4_t, acc[ai][1][m][1]), f32x4) * sr * sb[1][1]);
;                     u32x4 w; w.x = pk2(p0[0], p0[1]); w.y = pk2(p0[2], p0[3]); w.z = pk2(p1[0], p1[1]); w.w = pk2(p1[2], p1[3]);
;                     *(u32x4*)(base + (size_t)r * ldc + col0) = w; }
;             return; }
	v_pk_mul_f32 v[108:109], v[224:225], v[108:109] op_sel_hi:[0,1]
	v_pk_mul_f32 v[106:107], v[64:65], v[106:107]
	v_pk_mul_f32 v[108:109], v[66:67], v[108:109]
	v_pk_mul_f32 v[96:97], v[68:69], v[96:97]
	v_pk_mul_f32 v[98:99], v[70:71], v[98:99]
	s_nop 0
	v_pk_mul_f32 v[104:105], v[108:109], v[98:99]
	v_pk_mul_f32 v[98:99], v[106:107], v[96:97]
	v_cvt_pk_bf16_f32 v96, v100, v101
	v_mad_u64_u32 v[100:101], s[2:3], v175, s35, 0
	v_cvt_pk_bf16_f32 v97, v102, v103
	v_mov_b32_e32 v102, v101
	v_mad_u64_u32 v[102:103], s[2:3], v110, s35, v[102:103]
	v_mov_b32_e32 v101, v102
	v_cvt_pk_bf16_f32 v98, v98, v99
	v_cvt_pk_bf16_f32 v99, v104, v105
	v_lshl_add_u64 v[100:101], v[100:101], 1, v[148:149]
	global_store_dwordx4 v[100:101], v[96:99], off
	v_cvt_f32_i32_e32 v101, v15
	s_nop 0
	v_cvt_f32_i32_e32 v99, v13
	v_cvt_f32_i32_e32 v98, v12
	v_cvt_f32_i32_e32 v100, v14
	v_ashrrev_i32_e32 v102, 31, v174
	v_pk_mul_f32 v[100:101], v[226:227], v[100:101] op_sel_hi:[0,1]
	v_pk_mul_f32 v[98:99], v[226:227], v[98:99] op_sel_hi:[0,1]
	v_pk_mul_f32 v[94:95], v[226:227], v[94:95] op_sel_hi:[0,1]
	v_pk_mul_f32 v[92:93], v[226:227], v[92:93] op_sel_hi:[0,1]
	v_pk_mul_f32 v[98:99], v[72:73], v[98:99]
	v_pk_mul_f32 v[100:101], v[74:75], v[100:101]
	v_pk_mul_f32 v[92:93], v[76:77], v[92:93]
	v_pk_mul_f32 v[94:95], v[78:79], v[94:95]
	v_pk_mul_f32 v[92:93], v[98:99], v[92:93]
	v_pk_mul_f32 v[94:95], v[100:101], v[94:95]
	v_cvt_f32_i32_e32 v99, v9
	v_cvt_f32_i32_e32 v98, v8
	v_cvt_f32_i32_e32 v101, v11
	v_cvt_f32_i32_e32 v100, v10
	v_pk_mul_f32 v[90:91], v[226:227], v[90:91] op_sel_hi:[0,1]
	v_pk_mul_f32 v[98:99], v[226:227], v[98:99] op_sel_hi:[0,1]
	v_pk_mul_f32 v[88:89], v[226:227], v[88:89] op_sel_hi:[0,1]
	v_pk_mul_f32 v[100:101], v[226:227], v[100:101] op_sel_hi:[0,1]
	v_pk_mul_f32 v[98:99], v[64:65], v[98:99]
	v_pk_mul_f32 v[100:101], v[66:67], v[100:101]
	v_pk_mul_f32 v[88:89], v[68:69], v[88:89]
	v_pk_mul_f32 v[90:91], v[70:71], v[90:91]
	s_nop 0
	v_pk_mul_f32 v[96:97], v[100:101], v[90:91]
	v_pk_mul_f32 v[90:91], v[98:99], v[88:89]
	v_cvt_pk_bf16_f32 v88, v92, v93
	v_mad_u64_u32 v[92:93], s[2:3], v174, s35, 0
	v_cvt_pk_bf16_f32 v89, v94, v95
	v_mov_b32_e32 v94, v93
	v_mad_u64_u32 v[94:95], s[2:3], v102, s35, v[94:95]
	v_mov_b32_e32 v93, v94
	v_cvt_pk_bf16_f32 v90, v90, v91
	v_cvt_pk_bf16_f32 v91, v96, v97
	v_lshl_add_u64 v[92:93], v[92:93], 1, v[148:149]
	global_store_dwordx4 v[92:93], v[88:91], off
	v_cvt_f32_i32_e32 v93, v7
	s_nop 0
	v_cvt_f32_i32_e32 v91, v5
	v_cvt_f32_i32_e32 v90, v4
	v_cvt_f32_i32_e32 v92, v6
	v_ashrrev_i32_e32 v89, 31, v173
	v_pk_mul_f32 v[92:93], v[228:229], v[92:93] op_sel_hi:[0,1]
	v_pk_mul_f32 v[90:91], v[228:229], v[90:91] op_sel_hi:[0,1]
	v_pk_mul_f32 v[86:87], v[228:229], v[86:87] op_sel_hi:[0,1]
	v_pk_mul_f32 v[84:85], v[228:229], v[84:85] op_sel_hi:[0,1]
	v_pk_mul_f32 v[72:73], v[72:73], v[90:91]
	v_pk_mul_f32 v[74:75], v[74:75], v[92:93]
	v_pk_mul_f32 v[76:77], v[76:77], v[84:85]
	v_pk_mul_f32 v[78:79], v[78:79], v[86:87]
	v_pk_mul_f32 v[72:73], v[72:73], v[76:77]
	v_pk_mul_f32 v[74:75], v[74:75], v[78:79]
	v_cvt_f32_i32_e32 v77, v1
	v_cvt_f32_i32_e32 v76, v0
	v_cvt_f32_i32_e32 v79, v3
	v_cvt_f32_i32_e32 v78, v2
	v_pk_mul_f32 v[76:77], v[228:229], v[76:77] op_sel_hi:[0,1]
	v_pk_mul_f32 v[64:65], v[64:65], v[76:77]
	v_pk_mul_f32 v[78:79], v[228:229], v[78:79] op_sel_hi:[0,1]
	v_pk_mul_f32 v[66:67], v[66:67], v[78:79]
	v_pk_mul_f32 v[76:77], v[228:229], v[82:83] op_sel_hi:[0,1]
	v_pk_mul_f32 v[78:79], v[228:229], v[80:81] op_sel_hi:[0,1]
	v_pk_mul_f32 v[68:69], v[68:69], v[78:79]
	v_pk_mul_f32 v[70:71], v[70:71], v[76:77]
	s_nop 0
	v_pk_mul_f32 v[70:71], v[66:67], v[70:71]
	v_pk_mul_f32 v[66:67], v[64:65], v[68:69]
	v_mad_u64_u32 v[68:69], s[2:3], v173, s35, 0
	v_cvt_pk_bf16_f32 v66, v66, v67
	v_cvt_pk_bf16_f32 v67, v70, v71
	v_mov_b32_e32 v70, v69
	v_mad_u64_u32 v[70:71], s[2:3], v89, s35, v[70:71]
	v_mov_b32_e32 v69, v70
	v_cvt_pk_bf16_f32 v64, v72, v73
	v_cvt_pk_bf16_f32 v65, v74, v75
	v_lshl_add_u64 v[68:69], v[68:69], 1, v[148:149]
	global_store_dwordx4 v[68:69], v[64:67], off
